# cvt_wg tile-address blocks: dead reloads of 14 of the 16 kernarg pointer words per block removed
# speedup vs baseline: 1.0154x; 1.0154x over previous
.LBB0_573:
	s_or_b64 exec, exec, s[0:1]
	v_mov_b32_e32 v1, s46
	v_mov_b32_e32 v2, s3
	s_waitcnt lgkmcnt(0)
	s_barrier
	ds_read_b32 v1, v1
	ds_read_b32 v2, v2
	s_mov_b64 s[0:1], -1
	s_waitcnt lgkmcnt(1)
	v_readfirstlane_b32 s40, v1
	s_waitcnt lgkmcnt(0)
	v_cmp_lt_i32_e32 vcc, -1, v2
	v_readfirstlane_b32 s9, v2
	s_cbranch_vccz .LBB0_554
	s_lshl_b32 s0, s40, 7
	s_add_i32 s2, s9, s0
	v_readlane_b32 s0, v254, 63
	v_readlane_b32 s1, v255, 0
	s_mul_i32 s8, s2, 24
	s_andn2_b64 vcc, exec, s[0:1]
	s_mul_i32 s50, s40, 0x6000
	s_mul_i32 s51, s9, 0xc0
	s_mul_i32 s48, s40, 0x60000
	s_mul_i32 s49, s9, 0xc00
	s_barrier
	s_cbranch_vccnz .LBB0_632
	s_cmpk_gt_i32 s2, 0x2aa
	s_cselect_b64 s[0:1], -1, 0
	s_mov_b64 s[16:17], -1
	s_and_b64 vcc, exec, s[0:1]
	s_mulk_i32 s2, 0xc0
	s_cbranch_vccz .LBB0_577
	s_add_i32 s4, s8, 0xffffc000
	v_readlane_b32 s56, v254, 35
	v_readlane_b32 s57, v254, 36
	s_lshr_b32 s42, s4, 8
	s_lshl_b32 s4, s9, 10
	v_readlane_b32 s58, v254, 37
	v_readlane_b32 s59, v254, 38
	v_readlane_b32 s60, v254, 39
	v_readlane_b32 s61, v254, 40
	v_readlane_b32 s62, v254, 41
	v_readlane_b32 s63, v254, 42
	v_readlane_b32 s64, v254, 43
	v_readlane_b32 s65, v254, 44
	v_readlane_b32 s66, v254, 45
	v_readlane_b32 s67, v254, 46
	s_mov_b64 s[20:21], s[56:57]
	s_and_b32 s12, s2, 0x780
	s_and_b32 s16, s4, 0x400
	s_lshl_b64 s[14:15], s[42:43], 11
	s_lshl_b64 s[4:5], s[42:43], 24
	s_mov_b64 s[28:29], s[64:65]
	s_add_u32 s4, s28, s4
	s_addc_u32 s5, s29, s5
	s_lshl_b32 s10, s12, 13
	s_add_u32 s4, s4, s10
	s_addc_u32 s5, s5, 0
	s_lshl_b32 s10, s16, 2
	s_add_u32 s10, s4, s10
	s_mov_b64 s[22:23], s[58:59]
	s_mov_b64 s[24:25], s[60:61]
	s_mov_b64 s[26:27], s[62:63]
	s_mov_b64 s[30:31], s[66:67]
	s_mov_b32 s13, s43
	s_addc_u32 s11, s5, 0
	s_or_b32 s14, s14, s16
	s_mov_b64 s[16:17], 0
.LBB0_577:
	s_andn2_b64 vcc, exec, s[16:17]
	s_cbranch_vccnz .LBB0_579
	s_ashr_i32 s4, s8, 31
	s_lshr_b32 s4, s4, 23
	s_add_i32 s5, s8, s4
	s_ashr_i32 s4, s5, 9
	s_and_b32 s5, s5, 0xfe00
	s_sub_i32 s5, s8, s5
	s_sext_i32_i16 s10, s5
	s_bfe_u32 s10, s10, 0x5001a
	s_add_i32 s10, s5, s10
	s_sext_i32_i16 s11, s10
	s_and_b32 s10, s10, 0xffe0
	s_sub_i32 s5, s5, s10
	s_lshl_b32 s11, s11, 2
	s_sext_i32_i16 s5, s5
	s_and_b32 s12, s11, 0xffffff80
	s_lshl_b32 s11, s5, 8
	s_lshl_b32 s10, s5, 7
	s_and_b32 s11, s11, 0xf00
	s_cmp_gt_i32 s5, 15
	s_cselect_b32 s5, 0x80, 0
	v_readlane_b32 s56, v254, 35
	v_readlane_b32 s57, v254, 36
	s_or_b32 s16, s11, s5
	s_ashr_i32 s5, s4, 31
	v_readlane_b32 s58, v254, 37
	v_readlane_b32 s59, v254, 38
	v_readlane_b32 s60, v254, 39
	v_readlane_b32 s61, v254, 40
	v_readlane_b32 s62, v254, 41
	v_readlane_b32 s63, v254, 42
	v_readlane_b32 s64, v254, 43
	v_readlane_b32 s65, v254, 44
	v_readlane_b32 s66, v254, 45
	v_readlane_b32 s67, v254, 46
	s_mov_b64 s[20:21], s[56:57]
	s_lshl_b64 s[14:15], s[4:5], 25
	s_mov_b64 s[24:25], s[60:61]
	s_add_u32 s11, s24, s14
	s_addc_u32 s17, s25, s15
	s_ashr_i32 s13, s12, 31
	s_lshl_b64 s[14:15], s[12:13], 14
	s_add_u32 s14, s11, s14
	s_addc_u32 s15, s17, s15
	s_ashr_i32 s11, s10, 31
	s_lshl_b64 s[10:11], s[10:11], 2
	s_add_u32 s10, s14, s10
	s_addc_u32 s11, s15, s11
	s_lshl_b64 s[14:15], s[4:5], 12
	s_or_b32 s14, s14, s16
	s_mov_b64 s[18:19], 0x1000
	s_mov_b64 s[16:17], 0x5600000
	s_mov_b64 s[22:23], s[58:59]
	s_mov_b64 s[26:27], s[62:63]
	s_mov_b64 s[28:29], s[64:65]
	s_mov_b64 s[30:31], s[66:67]
	s_branch .LBB0_580

.LBB0_580:
	s_waitcnt vmcnt(9)
	v_mad_u64_u32 v[4:5], s[4:5], s18, v192, 0
	v_lshl_add_u64 v[4:5], v[4:5], 2, s[10:11]
	v_lshlrev_b32_e32 v2, 2, v194
	s_waitcnt vmcnt(5)
	v_lshl_add_u64 v[20:21], v[4:5], 0, v[2:3]
	s_lshl_b32 s42, s18, 2
	v_lshl_add_u64 v[12:13], v[20:21], 0, s[42:43]
	s_lshl_b32 s4, s18, 3
	v_lshl_add_u64 v[16:17], v[12:13], 0, s[42:43]
	s_sub_u32 s4, 0, s4
	s_waitcnt vmcnt(4)
	v_lshl_add_u64 v[24:25], v[16:17], 0, s[42:43]
	s_subb_u32 s5, 0, 0
	s_waitcnt vmcnt(3)
	v_lshl_add_u64 v[28:29], v[24:25], 0, s[4:5]
	s_waitcnt vmcnt(2)
	v_lshl_add_u64 v[32:33], v[28:29], 0, s[42:43]
	global_load_dwordx4 v[4:7], v[20:21], off nt
	global_load_dwordx4 v[8:11], v[12:13], off nt
	s_or_b32 s4, s8, 1
	global_load_dwordx4 v[12:15], v[16:17], off nt
	s_nop 0
	global_load_dwordx4 v[16:19], v[24:25], off nt
	s_nop 0
	global_load_dwordx4 v[20:23], v[20:21], off offset:256 nt
	s_mov_b64 s[20:21], -1
	global_load_dwordx4 v[24:27], v[28:29], off offset:256 nt
	s_and_b64 vcc, exec, s[0:1]
	global_load_dwordx4 v[28:31], v[32:33], off offset:256 nt
	v_lshl_add_u64 v[32:33], v[32:33], 0, s[42:43]
	global_load_dwordx4 v[32:35], v[32:33], off offset:256 nt
	s_cbranch_vccz .LBB0_582
	s_add_i32 s5, s8, 0xffffc001
	s_lshr_b32 s42, s5, 8
	s_lshl_b32 s5, s4, 7
	s_and_b32 s10, s2, 0x780
	s_and_b32 s5, s5, 0x480
	s_lshl_b64 s[18:19], s[42:43], 11
	s_lshl_b64 s[20:21], s[42:43], 24
	v_readlane_b32 s64, v254, 43
	v_readlane_b32 s65, v254, 44
	s_add_u32 s20, s64, s20
	s_addc_u32 s21, s65, s21
	s_lshl_b32 s22, s10, 13
	s_add_u32 s20, s20, s22
	s_addc_u32 s21, s21, 0
	s_lshl_b32 s22, s5, 2
	s_add_u32 s22, s20, s22
	s_mov_b32 s11, s43
	s_addc_u32 s23, s21, 0
	s_or_b32 s18, s18, s5
	s_mov_b64 s[20:21], 0
.LBB0_582:
	s_andn2_b64 vcc, exec, s[20:21]
	s_cbranch_vccnz .LBB0_584
	s_ashr_i32 s5, s4, 31
	s_lshr_b32 s5, s5, 23
	s_add_i32 s5, s4, s5
	s_ashr_i32 s18, s5, 9
	s_and_b32 s5, s5, 0xfe00
	s_sub_i32 s4, s4, s5
	s_sext_i32_i16 s5, s4
	s_bfe_u32 s5, s5, 0x5001a
	s_add_i32 s5, s4, s5
	s_sext_i32_i16 s10, s5
	s_and_b32 s5, s5, 0xffe0
	s_sub_i32 s4, s4, s5
	s_sext_i32_i16 s5, s4
	s_lshl_b32 s10, s10, 2
	s_lshl_b32 s11, s5, 8
	s_and_b32 s10, s10, 0xffffff80
	s_lshl_b32 s4, s5, 7
	s_and_b32 s11, s11, 0xf00
	s_cmp_gt_i32 s5, 15
	s_cselect_b32 s5, 0x80, 0
	s_ashr_i32 s19, s18, 31
	s_or_b32 s24, s11, s5
	s_lshl_b64 s[20:21], s[18:19], 25
	v_readlane_b32 s60, v254, 39
	v_readlane_b32 s61, v254, 40
	s_add_u32 s5, s60, s20
	s_addc_u32 s22, s61, s21
	s_ashr_i32 s11, s10, 31
	s_lshl_b64 s[20:21], s[10:11], 14
	s_add_u32 s20, s5, s20
	s_addc_u32 s21, s22, s21
	s_ashr_i32 s5, s4, 31
	s_lshl_b64 s[4:5], s[4:5], 2
	s_add_u32 s22, s20, s4
	s_addc_u32 s23, s21, s5
	s_lshl_b64 s[18:19], s[18:19], 12
	s_or_b32 s18, s18, s24
	s_mov_b64 s[24:25], 0x1000
	s_mov_b64 s[20:21], 0x5600000
	s_branch .LBB0_585

.LBB0_585:
	v_mad_u64_u32 v[36:37], s[4:5], s24, v192, 0
	v_lshl_add_u64 v[36:37], v[36:37], 2, s[22:23]
	v_lshl_add_u64 v[48:49], v[36:37], 0, v[2:3]
	s_lshl_b32 s42, s24, 2
	v_lshl_add_u64 v[44:45], v[48:49], 0, s[42:43]
	s_lshl_b32 s4, s24, 3
	v_lshl_add_u64 v[50:51], v[44:45], 0, s[42:43]
	s_sub_u32 s4, 0, s4
	v_lshl_add_u64 v[56:57], v[50:51], 0, s[42:43]
	s_subb_u32 s5, 0, 0
	v_lshl_add_u64 v[60:61], v[56:57], 0, s[4:5]
	v_lshl_add_u64 v[64:65], v[60:61], 0, s[42:43]
	global_load_dwordx4 v[36:39], v[48:49], off nt
	global_load_dwordx4 v[40:43], v[44:45], off nt
	s_or_b32 s4, s8, 2
	global_load_dwordx4 v[44:47], v[50:51], off nt
	global_load_dwordx4 v[52:55], v[56:57], off nt
	s_nop 0
	global_load_dwordx4 v[48:51], v[48:49], off offset:256 nt
	s_mov_b64 s[26:27], -1
	global_load_dwordx4 v[56:59], v[60:61], off offset:256 nt
	s_and_b64 vcc, exec, s[0:1]
	global_load_dwordx4 v[60:63], v[64:65], off offset:256 nt
	v_lshl_add_u64 v[64:65], v[64:65], 0, s[42:43]
	global_load_dwordx4 v[64:67], v[64:65], off offset:256 nt
	s_cbranch_vccz .LBB0_587
	s_add_i32 s5, s8, 0xffffc002
	s_lshr_b32 s42, s5, 8
	s_lshl_b32 s5, s4, 7
	s_and_b32 s22, s2, 0x780
	s_and_b32 s5, s5, 0x500
	s_lshl_b64 s[24:25], s[42:43], 11
	s_lshl_b64 s[26:27], s[42:43], 24
	v_readlane_b32 s64, v254, 43
	v_readlane_b32 s65, v254, 44
	s_add_u32 s26, s64, s26
	s_addc_u32 s27, s65, s27
	s_lshl_b32 s28, s22, 13
	s_add_u32 s26, s26, s28
	s_addc_u32 s27, s27, 0
	s_lshl_b32 s28, s5, 2
	s_add_u32 s28, s26, s28
	s_mov_b32 s23, s43
	s_addc_u32 s29, s27, 0
	s_or_b32 s24, s24, s5
	s_mov_b64 s[26:27], 0
.LBB0_587:
	s_andn2_b64 vcc, exec, s[26:27]
	s_cbranch_vccnz .LBB0_589
	s_ashr_i32 s5, s4, 31
	s_lshr_b32 s5, s5, 23
	s_add_i32 s5, s4, s5
	s_ashr_i32 s24, s5, 9
	s_and_b32 s5, s5, 0xfe00
	s_sub_i32 s4, s4, s5
	s_sext_i32_i16 s5, s4
	s_bfe_u32 s5, s5, 0x5001a
	s_add_i32 s5, s4, s5
	s_sext_i32_i16 s22, s5
	s_and_b32 s5, s5, 0xffe0
	s_sub_i32 s4, s4, s5
	s_sext_i32_i16 s5, s4
	s_lshl_b32 s22, s22, 2
	s_lshl_b32 s23, s5, 8
	s_and_b32 s22, s22, 0xffffff80
	s_lshl_b32 s4, s5, 7
	s_and_b32 s23, s23, 0xf00
	s_cmp_gt_i32 s5, 15
	s_cselect_b32 s5, 0x80, 0
	s_ashr_i32 s25, s24, 31
	s_or_b32 s30, s23, s5
	s_lshl_b64 s[26:27], s[24:25], 25
	v_readlane_b32 s60, v254, 39
	v_readlane_b32 s61, v254, 40
	s_add_u32 s5, s60, s26
	s_addc_u32 s28, s61, s27
	s_ashr_i32 s23, s22, 31
	s_lshl_b64 s[26:27], s[22:23], 14
	s_add_u32 s26, s5, s26
	s_addc_u32 s27, s28, s27
	s_ashr_i32 s5, s4, 31
	s_lshl_b64 s[4:5], s[4:5], 2
	s_add_u32 s28, s26, s4
	s_addc_u32 s29, s27, s5
	s_lshl_b64 s[24:25], s[24:25], 12
	s_or_b32 s24, s24, s30
	s_mov_b64 s[30:31], 0x1000
	s_mov_b64 s[26:27], 0x5600000
	s_branch .LBB0_590

.LBB0_590:
	v_mad_u64_u32 v[68:69], s[4:5], s30, v192, 0
	v_lshl_add_u64 v[68:69], v[68:69], 2, s[28:29]
	v_lshl_add_u64 v[80:81], v[68:69], 0, v[2:3]
	s_lshl_b32 s42, s30, 2
	v_lshl_add_u64 v[76:77], v[80:81], 0, s[42:43]
	s_lshl_b32 s4, s30, 3
	v_lshl_add_u64 v[82:83], v[76:77], 0, s[42:43]
	s_sub_u32 s4, 0, s4
	v_lshl_add_u64 v[88:89], v[82:83], 0, s[42:43]
	s_subb_u32 s5, 0, 0
	v_lshl_add_u64 v[92:93], v[88:89], 0, s[4:5]
	v_lshl_add_u64 v[96:97], v[92:93], 0, s[42:43]
	global_load_dwordx4 v[68:71], v[80:81], off nt
	global_load_dwordx4 v[72:75], v[76:77], off nt
	s_or_b32 s4, s8, 3
	global_load_dwordx4 v[76:79], v[82:83], off nt
	global_load_dwordx4 v[84:87], v[88:89], off nt
	s_nop 0
	global_load_dwordx4 v[80:83], v[80:81], off offset:256 nt
	s_mov_b64 s[36:37], -1
	global_load_dwordx4 v[88:91], v[92:93], off offset:256 nt
	s_and_b64 vcc, exec, s[0:1]
	global_load_dwordx4 v[92:95], v[96:97], off offset:256 nt
	v_lshl_add_u64 v[96:97], v[96:97], 0, s[42:43]
	global_load_dwordx4 v[96:99], v[96:97], off offset:256 nt
	s_cbranch_vccz .LBB0_592
	s_add_i32 s0, s8, 0xffffc003
	s_lshr_b32 s42, s0, 8
	s_lshl_b32 s0, s4, 7
	s_and_b32 s28, s2, 0x780
	s_and_b32 s2, s0, 0x580
	s_lshl_b64 s[34:35], s[42:43], 11
	s_lshl_b64 s[0:1], s[42:43], 24
	v_readlane_b32 s64, v254, 43
	v_readlane_b32 s65, v254, 44
	s_add_u32 s0, s64, s0
	s_addc_u32 s1, s65, s1
	s_lshl_b32 s5, s28, 13
	s_add_u32 s0, s0, s5
	s_addc_u32 s1, s1, 0
	s_lshl_b32 s5, s2, 2
	s_add_u32 s30, s0, s5
	s_mov_b32 s29, s43
	s_addc_u32 s31, s1, 0
	s_or_b32 s34, s34, s2
	s_mov_b64 s[36:37], 0
.LBB0_592:
	s_andn2_b64 vcc, exec, s[36:37]
	s_cbranch_vccnz .LBB0_594
	s_ashr_i32 s0, s4, 31
	s_lshr_b32 s0, s0, 23
	s_add_i32 s1, s4, s0
	s_ashr_i32 s0, s1, 9
	s_and_b32 s1, s1, 0xfe00
	s_sub_i32 s1, s4, s1
	s_sext_i32_i16 s2, s1
	s_bfe_u32 s2, s2, 0x5001a
	s_add_i32 s2, s1, s2
	s_sext_i32_i16 s4, s2
	s_and_b32 s2, s2, 0xffe0
	s_sub_i32 s1, s1, s2
	s_sext_i32_i16 s1, s1
	s_lshl_b32 s4, s4, 2
	s_lshl_b32 s2, s1, 8
	s_and_b32 s28, s4, 0xffffff80
	s_lshl_b32 s4, s1, 7
	s_and_b32 s2, s2, 0xf00
	s_cmp_gt_i32 s1, 15
	s_cselect_b32 s1, 0x80, 0
	s_or_b32 s2, s2, s1
	s_ashr_i32 s1, s0, 31
	s_lshl_b64 s[30:31], s[0:1], 25
	v_readlane_b32 s60, v254, 39
	v_readlane_b32 s61, v254, 40
	s_add_u32 s5, s60, s30
	s_addc_u32 s34, s61, s31
	s_ashr_i32 s29, s28, 31
	s_lshl_b64 s[30:31], s[28:29], 14
	s_add_u32 s30, s5, s30
	s_addc_u32 s31, s34, s31
	s_ashr_i32 s5, s4, 31
	s_lshl_b64 s[4:5], s[4:5], 2
	s_add_u32 s30, s30, s4
	s_addc_u32 s31, s31, s5
	s_lshl_b64 s[34:35], s[0:1], 12
	s_or_b32 s34, s34, s2
	s_mov_b64 s[36:37], 0x1000
	s_mov_b64 s[38:39], 0x5600000
	s_branch .LBB0_595

.LBB0_596:
	s_ashr_i32 s18, s5, 31
	s_lshr_b32 s18, s18, 23
	s_add_i32 s18, s5, s18
	s_ashr_i32 s22, s18, 9
	s_and_b32 s18, s18, 0xfe00
	s_sub_i32 s5, s5, s18
	s_sext_i32_i16 s18, s5
	s_bfe_u32 s18, s18, 0x5001a
	s_add_i32 s19, s5, s18
	s_sext_i32_i16 s18, s19
	s_and_b32 s19, s19, 0xffe0
	s_sub_i32 s5, s5, s19
	s_sext_i32_i16 s5, s5
	s_lshl_b32 s18, s18, 2
	s_lshl_b32 s19, s5, 8
	s_and_b32 s18, s18, 0xffffff80
	s_lshl_b32 s20, s5, 7
	s_and_b32 s19, s19, 0xf00
	s_cmp_gt_i32 s5, 15
	s_cselect_b32 s5, 0x80, 0
	s_ashr_i32 s23, s22, 31
	s_or_b32 s5, s19, s5
	s_lshl_b64 s[24:25], s[22:23], 25
	v_readlane_b32 s60, v254, 39
	v_readlane_b32 s61, v254, 40
	s_add_u32 s21, s60, s24
	s_addc_u32 s26, s61, s25
	s_ashr_i32 s19, s18, 31
	s_lshl_b64 s[24:25], s[18:19], 14
	s_add_u32 s24, s21, s24
	s_addc_u32 s25, s26, s25
	s_ashr_i32 s21, s20, 31
	s_lshl_b64 s[20:21], s[20:21], 2
	s_add_u32 s20, s24, s20
	s_addc_u32 s21, s25, s21
	s_lshl_b64 s[22:23], s[22:23], 12
	s_or_b32 s22, s22, s5
	s_mov_b64 s[24:25], 0x1000
	s_mov_b64 s[26:27], 0x5600000

.Lcv1_ld_0:
	s_add_i32 s27, s8, s5
	s_add_i32 s26, s27, 4
	s_cmpk_gt_i32 s26, 0x3fff
	s_mov_b64 s[24:25], -1
	s_cbranch_scc0 .LBB0_603
	s_addk_i32 s27, 0xc004
	s_lshr_b32 s42, s27, 8
	s_add_i32 s14, s2, 32
	s_add_i32 s15, s4, 0x200
	s_and_b32 s14, s14, 0x780
	s_and_b32 s24, s15, 0x600
	s_lshl_b64 s[22:23], s[42:43], 11
	s_lshl_b64 s[20:21], s[42:43], 24
	v_readlane_b32 s64, v254, 43
	v_readlane_b32 s65, v254, 44
	s_add_u32 s20, s64, s20
	s_addc_u32 s21, s65, s21
	s_lshl_b32 s25, s14, 13
	s_add_u32 s20, s20, s25
	s_addc_u32 s21, s21, 0
	s_lshl_b32 s25, s24, 2
	s_add_u32 s20, s20, s25
	s_mov_b32 s15, s43
	s_addc_u32 s21, s21, 0
	s_or_b32 s22, s22, s24
	s_mov_b64 s[24:25], 0
.LBB0_603:
	s_andn2_b64 vcc, exec, s[24:25]
	s_cbranch_vccnz .LBB0_605
	s_ashr_i32 s14, s26, 31
	s_lshr_b32 s14, s14, 23
	s_add_i32 s14, s26, s14
	s_ashr_i32 s22, s14, 9
	s_and_b32 s14, s14, 0xfe00
	s_sub_i32 s15, s26, s14
	s_sext_i32_i16 s14, s15
	s_bfe_u32 s14, s14, 0x5001a
	s_add_i32 s20, s15, s14
	s_sext_i32_i16 s14, s20
	s_and_b32 s20, s20, 0xffe0
	s_sub_i32 s15, s15, s20
	s_sext_i32_i16 s15, s15
	s_lshl_b32 s14, s14, 2
	s_lshl_b32 s21, s15, 8
	s_and_b32 s14, s14, 0xffffff80
	s_lshl_b32 s20, s15, 7
	s_and_b32 s21, s21, 0xf00
	s_cmp_gt_i32 s15, 15
	s_cselect_b32 s15, 0x80, 0
	s_ashr_i32 s23, s22, 31
	s_or_b32 s26, s21, s15
	s_lshl_b64 s[24:25], s[22:23], 25
	v_readlane_b32 s60, v254, 39
	v_readlane_b32 s61, v254, 40
	s_add_u32 s21, s60, s24
	s_addc_u32 s27, s61, s25
	s_ashr_i32 s15, s14, 31
	s_lshl_b64 s[24:25], s[14:15], 14
	s_add_u32 s24, s21, s24
	s_addc_u32 s25, s27, s25
	s_ashr_i32 s21, s20, 31
	s_lshl_b64 s[20:21], s[20:21], 2
	s_add_u32 s20, s24, s20
	s_addc_u32 s21, s25, s21
	s_lshl_b64 s[22:23], s[22:23], 12
	s_or_b32 s22, s22, s26
	s_mov_b64 s[24:25], 0x1000
	s_mov_b64 s[26:27], 0x5600000
	s_branch .LBB0_606

.Lcv1_ld_1:
	s_add_i32 s27, s8, s5
	s_add_i32 s26, s27, 5
	s_cmpk_gt_i32 s26, 0x3fff
	s_mov_b64 s[24:25], -1
	s_cbranch_scc0 .LBB0_613
	s_addk_i32 s27, 0xc005
	s_lshr_b32 s42, s27, 8
	s_add_i32 s18, s2, 40
	s_add_i32 s19, s4, 0x280
	s_and_b32 s18, s18, 0x780
	s_and_b32 s24, s19, 0x680
	s_lshl_b64 s[22:23], s[42:43], 11
	s_lshl_b64 s[20:21], s[42:43], 24
	v_readlane_b32 s64, v254, 43
	v_readlane_b32 s65, v254, 44
	s_add_u32 s20, s64, s20
	s_addc_u32 s21, s65, s21
	s_lshl_b32 s25, s18, 13
	s_add_u32 s20, s20, s25
	s_addc_u32 s21, s21, 0
	s_lshl_b32 s25, s24, 2
	s_add_u32 s20, s20, s25
	s_mov_b32 s19, s43
	s_addc_u32 s21, s21, 0
	s_or_b32 s22, s22, s24
	s_mov_b64 s[24:25], 0
.LBB0_613:
	s_andn2_b64 vcc, exec, s[24:25]
	s_cbranch_vccnz .LBB0_615
	s_ashr_i32 s18, s26, 31
	s_lshr_b32 s18, s18, 23
	s_add_i32 s18, s26, s18
	s_ashr_i32 s22, s18, 9
	s_and_b32 s18, s18, 0xfe00
	s_sub_i32 s19, s26, s18
	s_sext_i32_i16 s18, s19
	s_bfe_u32 s18, s18, 0x5001a
	s_add_i32 s20, s19, s18
	s_sext_i32_i16 s18, s20
	s_and_b32 s20, s20, 0xffe0
	s_sub_i32 s19, s19, s20
	s_sext_i32_i16 s19, s19
	s_lshl_b32 s18, s18, 2
	s_lshl_b32 s21, s19, 8
	s_and_b32 s18, s18, 0xffffff80
	s_lshl_b32 s20, s19, 7
	s_and_b32 s21, s21, 0xf00
	s_cmp_gt_i32 s19, 15
	s_cselect_b32 s19, 0x80, 0
	s_ashr_i32 s23, s22, 31
	s_or_b32 s26, s21, s19
	s_lshl_b64 s[24:25], s[22:23], 25
	v_readlane_b32 s60, v254, 39
	v_readlane_b32 s61, v254, 40
	s_add_u32 s21, s60, s24
	s_addc_u32 s27, s61, s25
	s_ashr_i32 s19, s18, 31
	s_lshl_b64 s[24:25], s[18:19], 14
	s_add_u32 s24, s21, s24
	s_addc_u32 s25, s27, s25
	s_ashr_i32 s21, s20, 31
	s_lshl_b64 s[20:21], s[20:21], 2
	s_add_u32 s20, s24, s20
	s_addc_u32 s21, s25, s21
	s_lshl_b64 s[22:23], s[22:23], 12
	s_or_b32 s22, s22, s26
	s_mov_b64 s[24:25], 0x1000
	s_mov_b64 s[26:27], 0x5600000
	s_branch .LBB0_616

.Lcv1_ld_2:
	s_add_i32 s27, s8, s5
	s_add_i32 s26, s27, 6
	s_cmpk_gt_i32 s26, 0x3fff
	s_mov_b64 s[24:25], -1
	s_cbranch_scc0 .LBB0_621
	s_addk_i32 s27, 0xc006
	s_lshr_b32 s42, s27, 8
	s_add_i32 s18, s2, 48
	s_add_i32 s19, s4, 0x300
	s_and_b32 s18, s18, 0x780
	s_and_b32 s24, s19, 0x700
	s_lshl_b64 s[22:23], s[42:43], 11
	s_lshl_b64 s[20:21], s[42:43], 24
	v_readlane_b32 s64, v254, 43
	v_readlane_b32 s65, v254, 44
	s_add_u32 s20, s64, s20
	s_addc_u32 s21, s65, s21
	s_lshl_b32 s25, s18, 13
	s_add_u32 s20, s20, s25
	s_addc_u32 s21, s21, 0
	s_lshl_b32 s25, s24, 2
	s_add_u32 s20, s20, s25
	s_mov_b32 s19, s43
	s_addc_u32 s21, s21, 0
	s_or_b32 s22, s22, s24
	s_mov_b64 s[24:25], 0

.Lcv1_ld_3:
	s_add_i32 s26, s8, s5
	s_add_i32 s5, s26, 7
	s_cmpk_gt_i32 s5, 0x3fff
	s_mov_b64 s[24:25], -1
	s_cbranch_scc0 .LBB0_629
	s_addk_i32 s26, 0xc007
	s_lshr_b32 s42, s26, 8
	s_add_i32 s18, s2, 56
	s_add_i32 s19, s4, 0x380
	s_and_b32 s18, s18, 0x780
	s_and_b32 s24, s19, 0x780
	s_lshl_b64 s[22:23], s[42:43], 11
	s_lshl_b64 s[20:21], s[42:43], 24
	v_readlane_b32 s64, v254, 43
	v_readlane_b32 s65, v254, 44
	s_add_u32 s20, s64, s20
	s_addc_u32 s21, s65, s21
	s_lshl_b32 s25, s18, 13
	s_add_u32 s20, s20, s25
	s_addc_u32 s21, s21, 0
	s_lshl_b32 s25, s24, 2
	s_add_u32 s20, s20, s25
	s_mov_b32 s19, s43
	s_addc_u32 s21, s21, 0
	s_or_b32 s22, s22, s24
	s_mov_b64 s[24:25], 0

.LBB0_734:
	v_mad_u64_u32 v[4:5], s[4:5], s10, v192, 0
	v_lshl_add_u64 v[4:5], v[4:5], 2, s[0:1]
	v_lshlrev_b32_e32 v2, 2, v194
	v_lshl_add_u64 v[16:17], v[4:5], 0, v[2:3]
	s_lshl_b32 s42, s10, 2
	v_lshl_add_u64 v[4:5], v[16:17], 0, s[42:43]
	s_lshl_b32 s0, s10, 3
	v_lshl_add_u64 v[12:13], v[4:5], 0, s[42:43]
	s_sub_u32 s0, 0, s0
	v_lshl_add_u64 v[20:21], v[12:13], 0, s[42:43]
	s_subb_u32 s1, 0, 0
	v_lshl_add_u64 v[28:29], v[20:21], 0, s[0:1]
	global_load_dwordx4 v[4:7], v[4:5], off nt
	s_nop 0
	global_load_dwordx4 v[8:11], v[12:13], off nt
	s_nop 0
	global_load_dwordx4 v[12:15], v[16:17], off nt
	s_nop 0
	global_load_dwordx4 v[16:19], v[16:17], off offset:256 nt
	s_nop 0
	global_load_dwordx4 v[20:23], v[20:21], off nt
	s_nop 0
	global_load_dwordx4 v[24:27], v[28:29], off offset:256 nt
	v_lshl_add_u64 v[28:29], v[28:29], 0, s[42:43]
	v_lshl_add_u64 v[32:33], v[28:29], 0, s[42:43]
	global_load_dwordx4 v[28:31], v[28:29], off offset:256 nt
	s_nop 0
	global_load_dwordx4 v[32:35], v[32:33], off offset:256 nt
	s_or_b32 s2, s8, 1
	s_cmpk_gt_i32 s8, 0x3ffe
	s_mov_b64 s[20:21], -1
	s_cbranch_scc0 .LBB0_736
	s_add_i32 s0, s8, 0xffffc001
	s_lshr_b32 s42, s0, 8
	s_lshl_b32 s0, s8, 3
	s_and_b32 s10, s0, 0x780
	s_lshl_b32 s0, s2, 7
	s_and_b32 s4, s0, 0x780
	s_lshl_b64 s[18:19], s[42:43], 11
	s_lshl_b64 s[0:1], s[42:43], 24
	v_readlane_b32 s64, v254, 43
	v_readlane_b32 s65, v254, 44
	s_add_u32 s0, s64, s0
	s_addc_u32 s1, s65, s1
	s_lshl_b32 s5, s10, 13
	s_add_u32 s0, s0, s5
	s_addc_u32 s1, s1, 0
	s_lshl_b32 s5, s4, 2
	s_add_u32 s0, s0, s5
	s_mov_b32 s11, s43
	s_addc_u32 s1, s1, 0
	s_or_b32 s18, s18, s4
	s_mov_b64 s[20:21], 0
.LBB0_736:
	s_andn2_b64 vcc, exec, s[20:21]
	s_cbranch_vccnz .LBB0_738
	s_ashr_i32 s0, s2, 31
	s_lshr_b32 s0, s0, 23
	s_add_i32 s0, s2, s0
	s_ashr_i32 s4, s0, 9
	s_and_b32 s0, s0, 0xfe00
	s_sub_i32 s0, s2, s0
	s_sext_i32_i16 s1, s0
	s_bfe_u32 s1, s1, 0x5001a
	s_add_i32 s1, s0, s1
	s_sext_i32_i16 s2, s1
	s_and_b32 s1, s1, 0xffe0
	s_sub_i32 s0, s0, s1
	s_lshl_b32 s2, s2, 2
	s_sext_i32_i16 s1, s0
	s_and_b32 s10, s2, 0xffffff80
	s_lshl_b32 s2, s1, 8
	s_lshl_b32 s0, s1, 7
	s_and_b32 s2, s2, 0xf00
	s_cmp_gt_i32 s1, 15
	s_cselect_b32 s1, 0x80, 0
	s_ashr_i32 s5, s4, 31
	s_or_b32 s2, s2, s1
	s_lshl_b64 s[18:19], s[4:5], 25
	v_readlane_b32 s60, v254, 39
	v_readlane_b32 s61, v254, 40
	s_add_u32 s1, s60, s18
	s_addc_u32 s9, s61, s19
	s_ashr_i32 s11, s10, 31
	s_lshl_b64 s[18:19], s[10:11], 14
	s_add_u32 s18, s1, s18
	s_addc_u32 s9, s9, s19
	s_ashr_i32 s1, s0, 31
	s_lshl_b64 s[0:1], s[0:1], 2
	s_add_u32 s0, s18, s0
	s_addc_u32 s1, s9, s1
	s_lshl_b64 s[18:19], s[4:5], 12
	s_or_b32 s18, s18, s2
	s_mov_b64 s[22:23], 0x1000
	s_mov_b64 s[20:21], 0x5600000
	s_branch .LBB0_739

.LBB0_739:
	v_mad_u64_u32 v[36:37], s[4:5], s22, v192, 0
	v_lshl_add_u64 v[36:37], v[36:37], 2, s[0:1]
	v_lshl_add_u64 v[48:49], v[36:37], 0, v[2:3]
	s_lshl_b32 s42, s22, 2
	v_lshl_add_u64 v[36:37], v[48:49], 0, s[42:43]
	s_lshl_b32 s0, s22, 3
	v_lshl_add_u64 v[44:45], v[36:37], 0, s[42:43]
	s_sub_u32 s0, 0, s0
	v_lshl_add_u64 v[52:53], v[44:45], 0, s[42:43]
	s_subb_u32 s1, 0, 0
	v_lshl_add_u64 v[60:61], v[52:53], 0, s[0:1]
	global_load_dwordx4 v[36:39], v[36:37], off nt
	s_nop 0
	global_load_dwordx4 v[40:43], v[44:45], off nt
	s_nop 0
	global_load_dwordx4 v[44:47], v[48:49], off nt
	s_nop 0
	global_load_dwordx4 v[48:51], v[48:49], off offset:256 nt
	s_nop 0
	global_load_dwordx4 v[52:55], v[52:53], off nt
	s_nop 0
	global_load_dwordx4 v[56:59], v[60:61], off offset:256 nt
	v_lshl_add_u64 v[60:61], v[60:61], 0, s[42:43]
	v_lshl_add_u64 v[64:65], v[60:61], 0, s[42:43]
	global_load_dwordx4 v[60:63], v[60:61], off offset:256 nt
	s_nop 0
	global_load_dwordx4 v[64:67], v[64:65], off offset:256 nt
	s_add_i32 s2, s8, 2
	s_cmpk_gt_i32 s8, 0x3ffd
	s_mov_b64 s[24:25], -1
	s_cbranch_scc0 .LBB0_741
	s_add_i32 s0, s8, 0xffffc002
	s_lshr_b32 s42, s0, 8
	s_lshl_b32 s0, s2, 3
	s_lshl_b32 s1, s2, 7
	s_and_b32 s0, s0, 0x780
	s_and_b32 s9, s1, 0x700
	s_lshl_b64 s[22:23], s[42:43], 11
	s_lshl_b64 s[4:5], s[42:43], 24
	v_readlane_b32 s64, v254, 43
	v_readlane_b32 s65, v254, 44
	s_add_u32 s4, s64, s4
	s_addc_u32 s5, s65, s5
	s_lshl_b32 s24, s0, 13
	s_add_u32 s4, s4, s24
	s_addc_u32 s5, s5, 0
	s_lshl_b32 s24, s9, 2
	s_add_u32 s26, s4, s24
	s_mov_b32 s1, s43
	s_addc_u32 s27, s5, 0
	s_or_b32 s22, s22, s9
	s_mov_b64 s[24:25], 0
.LBB0_741:
	s_andn2_b64 vcc, exec, s[24:25]
	s_cbranch_vccnz .LBB0_743
	s_ashr_i32 s0, s2, 31
	s_lshr_b32 s0, s0, 23
	s_add_i32 s0, s2, s0
	s_ashr_i32 s4, s0, 9
	s_and_b32 s0, s0, 0xfe00
	s_sub_i32 s1, s2, s0
	s_sext_i32_i16 s0, s1
	s_bfe_u32 s0, s0, 0x5001a
	s_add_i32 s2, s1, s0
	s_sext_i32_i16 s0, s2
	s_and_b32 s2, s2, 0xffe0
	s_sub_i32 s1, s1, s2
	s_sext_i32_i16 s1, s1
	s_lshl_b32 s0, s0, 2
	s_lshl_b32 s2, s1, 8
	s_and_b32 s0, s0, 0xffffff80
	s_lshl_b32 s22, s1, 7
	s_and_b32 s2, s2, 0xf00
	s_cmp_gt_i32 s1, 15
	s_cselect_b32 s1, 0x80, 0
	s_ashr_i32 s5, s4, 31
	s_or_b32 s2, s2, s1
	s_lshl_b64 s[24:25], s[4:5], 25
	v_readlane_b32 s60, v254, 39
	v_readlane_b32 s61, v254, 40
	s_add_u32 s9, s60, s24
	s_addc_u32 s23, s61, s25
	s_ashr_i32 s1, s0, 31
	s_lshl_b64 s[24:25], s[0:1], 14
	s_add_u32 s9, s9, s24
	s_addc_u32 s24, s23, s25
	s_ashr_i32 s23, s22, 31
	s_lshl_b64 s[22:23], s[22:23], 2
	s_add_u32 s26, s9, s22
	s_addc_u32 s27, s24, s23
	s_lshl_b64 s[22:23], s[4:5], 12
	s_or_b32 s22, s22, s2
	s_mov_b64 s[28:29], 0x1000
	s_mov_b64 s[24:25], 0x5600000
	s_branch .LBB0_744

.LBB0_744:
	v_mad_u64_u32 v[68:69], s[4:5], s28, v192, 0
	v_lshl_add_u64 v[68:69], v[68:69], 2, s[26:27]
	v_lshl_add_u64 v[80:81], v[68:69], 0, v[2:3]
	s_lshl_b32 s42, s28, 2
	v_lshl_add_u64 v[68:69], v[80:81], 0, s[42:43]
	s_lshl_b32 s2, s28, 3
	v_lshl_add_u64 v[76:77], v[68:69], 0, s[42:43]
	s_sub_u32 s4, 0, s2
	v_lshl_add_u64 v[84:85], v[76:77], 0, s[42:43]
	s_subb_u32 s5, 0, 0
	v_lshl_add_u64 v[92:93], v[84:85], 0, s[4:5]
	global_load_dwordx4 v[68:71], v[68:69], off nt
	s_nop 0
	global_load_dwordx4 v[72:75], v[76:77], off nt
	s_nop 0
	global_load_dwordx4 v[76:79], v[80:81], off nt
	s_nop 0
	global_load_dwordx4 v[80:83], v[80:81], off offset:256 nt
	s_nop 0
	global_load_dwordx4 v[84:87], v[84:85], off nt
	s_nop 0
	global_load_dwordx4 v[88:91], v[92:93], off offset:256 nt
	v_lshl_add_u64 v[92:93], v[92:93], 0, s[42:43]
	v_lshl_add_u64 v[96:97], v[92:93], 0, s[42:43]
	global_load_dwordx4 v[92:95], v[92:93], off offset:256 nt
	s_nop 0
	global_load_dwordx4 v[96:99], v[96:97], off offset:256 nt
	s_add_i32 s2, s8, 3
	s_cmpk_gt_i32 s8, 0x3ffc
	s_mov_b64 s[34:35], -1
	s_cbranch_scc0 .LBB0_746
	s_add_i32 s4, s8, 0xffffc003
	s_lshr_b32 s42, s4, 8
	s_lshl_b32 s4, s2, 3
	s_and_b32 s26, s4, 0x780
	s_lshl_b32 s4, s2, 7
	s_and_b32 s9, s4, 0x780
	s_lshl_b64 s[30:31], s[42:43], 11
	s_lshl_b64 s[4:5], s[42:43], 24
	v_readlane_b32 s64, v254, 43
	v_readlane_b32 s65, v254, 44
	s_add_u32 s4, s64, s4
	s_addc_u32 s5, s65, s5
	s_lshl_b32 s28, s26, 13
	s_add_u32 s4, s4, s28
	s_addc_u32 s5, s5, 0
	s_lshl_b32 s28, s9, 2
	s_add_u32 s28, s4, s28
	s_mov_b32 s27, s43
	s_addc_u32 s29, s5, 0
	s_or_b32 s30, s30, s9
	s_mov_b64 s[34:35], 0
.LBB0_746:
	s_andn2_b64 vcc, exec, s[34:35]
	s_cbranch_vccnz .LBB0_748
	s_ashr_i32 s4, s2, 31
	s_lshr_b32 s4, s4, 23
	s_add_i32 s5, s2, s4
	s_ashr_i32 s4, s5, 9
	s_and_b32 s5, s5, 0xfe00
	s_sub_i32 s2, s2, s5
	s_sext_i32_i16 s5, s2
	s_bfe_u32 s5, s5, 0x5001a
	s_add_i32 s5, s2, s5
	s_sext_i32_i16 s9, s5
	s_and_b32 s5, s5, 0xffe0
	s_sub_i32 s2, s2, s5
	s_sext_i32_i16 s2, s2
	s_lshl_b32 s9, s9, 2
	s_lshl_b32 s5, s2, 8
	s_and_b32 s26, s9, 0xffffff80
	s_lshl_b32 s28, s2, 7
	s_and_b32 s5, s5, 0xf00
	s_cmp_gt_i32 s2, 15
	s_cselect_b32 s2, 0x80, 0
	s_or_b32 s2, s5, s2
	s_ashr_i32 s5, s4, 31
	s_lshl_b64 s[30:31], s[4:5], 25
	v_readlane_b32 s60, v254, 39
	v_readlane_b32 s61, v254, 40
	s_add_u32 s9, s60, s30
	s_addc_u32 s29, s61, s31
	s_ashr_i32 s27, s26, 31
	s_lshl_b64 s[30:31], s[26:27], 14
	s_add_u32 s9, s9, s30
	s_addc_u32 s30, s29, s31
	s_ashr_i32 s29, s28, 31
	s_lshl_b64 s[28:29], s[28:29], 2
	s_add_u32 s28, s9, s28
	s_addc_u32 s29, s30, s29
	s_lshl_b64 s[30:31], s[4:5], 12
	s_or_b32 s30, s30, s2
	s_mov_b64 s[34:35], 0x1000
	s_mov_b64 s[36:37], 0x5600000
	s_branch .LBB0_749

.LBB0_750:
	s_ashr_i32 s18, s5, 31
	s_lshr_b32 s18, s18, 23
	s_add_i32 s18, s5, s18
	s_ashr_i32 s22, s18, 9
	s_and_b32 s18, s18, 0xfe00
	s_sub_i32 s5, s5, s18
	s_sext_i32_i16 s18, s5
	s_bfe_u32 s18, s18, 0x5001a
	s_add_i32 s19, s5, s18
	s_sext_i32_i16 s18, s19
	s_and_b32 s19, s19, 0xffe0
	s_sub_i32 s5, s5, s19
	s_sext_i32_i16 s5, s5
	s_lshl_b32 s18, s18, 2
	s_lshl_b32 s19, s5, 8
	s_and_b32 s18, s18, 0xffffff80
	s_lshl_b32 s20, s5, 7
	s_and_b32 s19, s19, 0xf00
	s_cmp_gt_i32 s5, 15
	s_cselect_b32 s5, 0x80, 0
	s_ashr_i32 s23, s22, 31
	v_readlane_b32 s48, v254, 31
	s_or_b32 s5, s19, s5
	s_lshl_b64 s[24:25], s[22:23], 25
	v_readlane_b32 s56, v254, 39
	v_readlane_b32 s57, v254, 40
	s_add_u32 s21, s56, s24
	s_addc_u32 s26, s57, s25
	s_ashr_i32 s19, s18, 31
	s_lshl_b64 s[24:25], s[18:19], 14
	s_add_u32 s24, s21, s24
	s_addc_u32 s25, s26, s25
	s_ashr_i32 s21, s20, 31
	s_lshl_b64 s[20:21], s[20:21], 2
	s_add_u32 s20, s24, s20
	s_addc_u32 s21, s25, s21
	s_lshl_b64 s[22:23], s[22:23], 12
	s_or_b32 s22, s22, s5
	s_mov_b64 s[24:25], 0x1000
	s_mov_b64 s[26:27], 0x5600000
	v_readlane_b32 s49, v254, 32
	v_readlane_b32 s50, v254, 33
	v_readlane_b32 s51, v254, 34
.LBB0_751:
	s_add_u32 s5, s92, s26
	s_mulk_i32 s23, 0x880
	s_mul_hi_u32 s26, s22, 0x880
	s_addc_u32 s25, s93, s27
	s_add_i32 s26, s26, s23
	s_mulk_i32 s22, 0x880
	s_add_u32 s5, s5, s22
	s_addc_u32 s22, s25, s26
	s_add_u32 s18, s5, s18
	s_addc_u32 s19, s22, s19
	v_mad_u64_u32 v[100:101], s[22:23], s24, v192, 0
	v_lshl_add_u64 v[100:101], v[100:101], 2, s[20:21]
	v_lshl_add_u64 v[112:113], v[100:101], 0, v[2:3]
	s_lshl_b32 s42, s24, 2
	v_lshl_add_u64 v[100:101], v[112:113], 0, s[42:43]
	s_lshl_b32 s5, s24, 3
	v_lshl_add_u64 v[108:109], v[100:101], 0, s[42:43]
	s_sub_u32 s20, 0, s5
	v_lshl_add_u64 v[116:117], v[108:109], 0, s[42:43]
	s_subb_u32 s21, 0, 0
	v_lshl_add_u64 v[124:125], v[116:117], 0, s[20:21]
	global_load_dwordx4 v[100:103], v[100:101], off nt
	s_nop 0
	global_load_dwordx4 v[104:107], v[108:109], off nt
	s_nop 0
	global_load_dwordx4 v[108:111], v[112:113], off nt
	s_nop 0
	global_load_dwordx4 v[112:115], v[112:113], off offset:256 nt
	s_nop 0
	global_load_dwordx4 v[116:119], v[116:117], off nt
	s_nop 0
	global_load_dwordx4 v[120:123], v[124:125], off offset:256 nt
	v_lshl_add_u64 v[124:125], v[124:125], 0, s[42:43]
	v_lshl_add_u64 v[128:129], v[124:125], 0, s[42:43]
	global_load_dwordx4 v[124:127], v[124:125], off offset:256 nt
	s_nop 0
	global_load_dwordx4 v[128:131], v[128:129], off offset:256 nt

.Lcv2_ld_0:
	s_add_i32 s27, s8, s5
	s_add_i32 s26, s27, 4
	s_cmpk_gt_i32 s26, 0x3fff
	s_mov_b64 s[24:25], -1
	s_cbranch_scc0 .LBB0_757
	s_addk_i32 s27, 0xc004
	s_lshr_b32 s42, s27, 8
	s_add_i32 s14, s2, 32
	s_add_i32 s15, s4, 0x200
	v_readlane_b32 s48, v254, 31
	s_and_b32 s14, s14, 0x780
	s_and_b32 s24, s15, 0x700
	s_lshl_b64 s[22:23], s[42:43], 11
	s_lshl_b64 s[20:21], s[42:43], 24
	v_readlane_b32 s60, v254, 43
	v_readlane_b32 s61, v254, 44
	s_add_u32 s20, s60, s20
	s_addc_u32 s21, s61, s21
	s_lshl_b32 s25, s14, 13
	s_add_u32 s20, s20, s25
	s_addc_u32 s21, s21, 0
	s_lshl_b32 s25, s24, 2
	s_add_u32 s20, s20, s25
	v_readlane_b32 s49, v254, 32
	v_readlane_b32 s50, v254, 33
	v_readlane_b32 s51, v254, 34
	s_mov_b32 s15, s43
	s_addc_u32 s21, s21, 0
	s_or_b32 s22, s22, s24
	s_mov_b64 s[24:25], 0
.LBB0_757:
	s_andn2_b64 vcc, exec, s[24:25]
	s_cbranch_vccnz .LBB0_759
	s_ashr_i32 s14, s26, 31
	s_lshr_b32 s14, s14, 23
	s_add_i32 s14, s26, s14
	s_ashr_i32 s22, s14, 9
	s_and_b32 s14, s14, 0xfe00
	s_sub_i32 s15, s26, s14
	s_sext_i32_i16 s14, s15
	s_bfe_u32 s14, s14, 0x5001a
	s_add_i32 s20, s15, s14
	s_sext_i32_i16 s14, s20
	s_and_b32 s20, s20, 0xffe0
	s_sub_i32 s15, s15, s20
	s_sext_i32_i16 s15, s15
	s_lshl_b32 s14, s14, 2
	s_lshl_b32 s21, s15, 8
	s_and_b32 s14, s14, 0xffffff80
	s_lshl_b32 s20, s15, 7
	s_and_b32 s21, s21, 0xf00
	s_cmp_gt_i32 s15, 15
	s_cselect_b32 s15, 0x80, 0
	s_ashr_i32 s23, s22, 31
	v_readlane_b32 s48, v254, 31
	s_or_b32 s26, s21, s15
	s_lshl_b64 s[24:25], s[22:23], 25
	v_readlane_b32 s56, v254, 39
	v_readlane_b32 s57, v254, 40
	s_add_u32 s21, s56, s24
	s_addc_u32 s27, s57, s25
	s_ashr_i32 s15, s14, 31
	s_lshl_b64 s[24:25], s[14:15], 14
	s_add_u32 s24, s21, s24
	s_addc_u32 s25, s27, s25
	s_ashr_i32 s21, s20, 31
	s_lshl_b64 s[20:21], s[20:21], 2
	s_add_u32 s20, s24, s20
	s_addc_u32 s21, s25, s21
	s_lshl_b64 s[22:23], s[22:23], 12
	s_or_b32 s22, s22, s26
	s_mov_b64 s[24:25], 0x1000
	s_mov_b64 s[26:27], 0x5600000
	v_readlane_b32 s49, v254, 32
	v_readlane_b32 s50, v254, 33
	v_readlane_b32 s51, v254, 34
	s_branch .LBB0_760

.Lcv2_ld_1:
	s_add_i32 s27, s8, s5
	s_add_i32 s26, s27, 5
	s_cmpk_gt_i32 s26, 0x3fff
	s_mov_b64 s[24:25], -1
	s_cbranch_scc0 .LBB0_767
	s_addk_i32 s27, 0xc005
	s_lshr_b32 s42, s27, 8
	s_add_i32 s18, s2, 40
	s_add_i32 s19, s4, 0x280
	v_readlane_b32 s48, v254, 31
	s_and_b32 s18, s18, 0x780
	s_and_b32 s24, s19, 0x780
	s_lshl_b64 s[22:23], s[42:43], 11
	s_lshl_b64 s[20:21], s[42:43], 24
	v_readlane_b32 s60, v254, 43
	v_readlane_b32 s61, v254, 44
	s_add_u32 s20, s60, s20
	s_addc_u32 s21, s61, s21
	s_lshl_b32 s25, s18, 13
	s_add_u32 s20, s20, s25
	s_addc_u32 s21, s21, 0
	s_lshl_b32 s25, s24, 2
	s_add_u32 s20, s20, s25
	v_readlane_b32 s49, v254, 32
	v_readlane_b32 s50, v254, 33
	v_readlane_b32 s51, v254, 34
	s_mov_b32 s19, s43
	s_addc_u32 s21, s21, 0
	s_or_b32 s22, s22, s24
	s_mov_b64 s[24:25], 0
.LBB0_767:
	s_andn2_b64 vcc, exec, s[24:25]
	s_cbranch_vccnz .LBB0_769
	s_ashr_i32 s18, s26, 31
	s_lshr_b32 s18, s18, 23
	s_add_i32 s18, s26, s18
	s_ashr_i32 s22, s18, 9
	s_and_b32 s18, s18, 0xfe00
	s_sub_i32 s19, s26, s18
	s_sext_i32_i16 s18, s19
	s_bfe_u32 s18, s18, 0x5001a
	s_add_i32 s20, s19, s18
	s_sext_i32_i16 s18, s20
	s_and_b32 s20, s20, 0xffe0
	s_sub_i32 s19, s19, s20
	s_sext_i32_i16 s19, s19
	s_lshl_b32 s18, s18, 2
	s_lshl_b32 s21, s19, 8
	s_and_b32 s18, s18, 0xffffff80
	s_lshl_b32 s20, s19, 7
	s_and_b32 s21, s21, 0xf00
	s_cmp_gt_i32 s19, 15
	s_cselect_b32 s19, 0x80, 0
	s_ashr_i32 s23, s22, 31
	v_readlane_b32 s48, v254, 31
	s_or_b32 s26, s21, s19
	s_lshl_b64 s[24:25], s[22:23], 25
	v_readlane_b32 s56, v254, 39
	v_readlane_b32 s57, v254, 40
	s_add_u32 s21, s56, s24
	s_addc_u32 s27, s57, s25
	s_ashr_i32 s19, s18, 31
	s_lshl_b64 s[24:25], s[18:19], 14
	s_add_u32 s24, s21, s24
	s_addc_u32 s25, s27, s25
	s_ashr_i32 s21, s20, 31
	s_lshl_b64 s[20:21], s[20:21], 2
	s_add_u32 s20, s24, s20
	s_addc_u32 s21, s25, s21
	s_lshl_b64 s[22:23], s[22:23], 12
	s_or_b32 s22, s22, s26
	s_mov_b64 s[24:25], 0x1000
	s_mov_b64 s[26:27], 0x5600000
	v_readlane_b32 s49, v254, 32
	v_readlane_b32 s50, v254, 33
	v_readlane_b32 s51, v254, 34
	s_branch .LBB0_770

.Lcv2_ld_2:
	s_add_i32 s27, s8, s5
	s_add_i32 s26, s27, 6
	s_cmpk_gt_i32 s26, 0x3fff
	s_mov_b64 s[24:25], -1
	s_cbranch_scc0 .LBB0_775
	s_addk_i32 s27, 0xc006
	s_lshr_b32 s42, s27, 8
	s_add_i32 s18, s2, 48
	s_add_i32 s19, s4, 0x300
	v_readlane_b32 s48, v254, 31
	s_and_b32 s18, s18, 0x780
	s_and_b32 s24, s19, 0x700
	s_lshl_b64 s[22:23], s[42:43], 11
	s_lshl_b64 s[20:21], s[42:43], 24
	v_readlane_b32 s60, v254, 43
	v_readlane_b32 s61, v254, 44
	s_add_u32 s20, s60, s20
	s_addc_u32 s21, s61, s21
	s_lshl_b32 s25, s18, 13
	s_add_u32 s20, s20, s25
	s_addc_u32 s21, s21, 0
	s_lshl_b32 s25, s24, 2
	s_add_u32 s20, s20, s25
	v_readlane_b32 s49, v254, 32
	v_readlane_b32 s50, v254, 33
	v_readlane_b32 s51, v254, 34
	s_mov_b32 s19, s43
	s_addc_u32 s21, s21, 0
	s_or_b32 s22, s22, s24
	s_mov_b64 s[24:25], 0

.Lcv2_ld_3:
	s_add_i32 s26, s8, s5
	s_add_i32 s5, s26, 7
	s_cmpk_gt_i32 s5, 0x3fff
	s_mov_b64 s[24:25], -1
	s_cbranch_scc0 .LBB0_783
	s_addk_i32 s26, 0xc007
	s_lshr_b32 s42, s26, 8
	s_add_i32 s18, s2, 56
	s_add_i32 s19, s4, 0x380
	v_readlane_b32 s48, v254, 31
	s_and_b32 s18, s18, 0x780
	s_and_b32 s24, s19, 0x780
	s_lshl_b64 s[22:23], s[42:43], 11
	s_lshl_b64 s[20:21], s[42:43], 24
	v_readlane_b32 s60, v254, 43
	v_readlane_b32 s61, v254, 44
	s_add_u32 s20, s60, s20
	s_addc_u32 s21, s61, s21
	s_lshl_b32 s25, s18, 13
	s_add_u32 s20, s20, s25
	s_addc_u32 s21, s21, 0
	s_lshl_b32 s25, s24, 2
	s_add_u32 s20, s20, s25
	v_readlane_b32 s49, v254, 32
	v_readlane_b32 s50, v254, 33
	v_readlane_b32 s51, v254, 34
	s_mov_b32 s19, s43
	s_addc_u32 s21, s21, 0
	s_or_b32 s22, s22, s24
	s_mov_b64 s[24:25], 0
